# speedup vs baseline: 1.0158x; 1.0158x over previous
_ZN12_GLOBAL__N_113search_kernelEPKfS1_PhPf:
	s_load_dwordx2 s[8:9], s[0:1], 0x0
	s_load_dwordx2 s[4:5], s[0:1], 0x10
	s_movk_i32 s3, 0x90
	v_readfirstlane_b32 s10, v0
	v_cmp_gt_u32_e32 vcc, s3, v0
	s_and_saveexec_b64 s[6:7], vcc
	v_mov_b32_e32 v2, -1
	v_lshlrev_b32_e32 v1, 3, v0
	v_mov_b32_e32 v3, v2
	ds_write_b64 v1, v[2:3] offset:16384
	s_or_b64 exec, exec, s[6:7]
	s_waitcnt lgkmcnt(0)
	s_add_u32 s6, s4, 0x240000
	s_addc_u32 s7, s5, 0
	s_lshl_b32 s11, s2, 1
	s_and_b32 s14, s11, 14
	s_ashr_i32 s11, s2, 7
	s_lshr_b32 s15, s10, 6
	s_add_i32 s14, s14, s11
	s_bfe_u32 s2, s2, 0x40003
	s_mul_i32 s11, s15, 24
	v_mul_u32_u24_e32 v2, 0x71d, v0
	v_mul_u32_u24_e32 v4, 0x195, v0
	s_min_u32 s18, s11, 0xa5
	s_mul_i32 s11, s14, 3
	s_mul_i32 s12, s2, 9
	s_mov_b32 s13, 0
	v_lshrrev_b32_e32 v3, 16, v2
	s_movk_i32 s19, 0xffdc
	v_lshrrev_b32_e32 v5, 17, v4
	v_mad_i32_i24 v2, v3, s19, v0
	v_mad_i32_i24 v4, v5, -9, v3
	v_add_u32_e32 v3, s11, v5
	v_mov_b64_e32 v[6:7], s[12:13]
	v_mad_i64_i32 v[8:9], s[16:17], v3, s3, v[6:7]
	v_ashrrev_i32_e32 v5, 31, v4
	v_lshl_add_u64 v[4:5], v[8:9], 0, v[4:5]
	s_movk_i32 s13, 0x240
	v_mov_b64_e32 v[8:9], s[8:9]
	v_mad_u64_u32 v[10:11], s[8:9], v4, s13, v[8:9]
	v_min_u32_e32 v4, 0x1cb, v0
	v_or_b32_e32 v4, 0x200, v4
	v_mad_i32_i24 v11, v5, s13, v11
	v_mul_u32_u24_e32 v5, 0x71d, v4
	v_ashrrev_i32_e32 v3, 31, v2
	v_lshrrev_b32_e32 v5, 16, v5
	v_lshl_add_u64 v[2:3], v[2:3], 4, v[10:11]
	v_mad_i32_i24 v10, v5, s19, v4
	v_mul_u32_u24_e32 v4, 0x653, v4
	v_lshrrev_b32_e32 v11, 19, v4
	v_mad_i32_i24 v4, v11, -9, v5
	v_add_u32_e32 v5, s11, v11
	v_mad_i64_i32 v[6:7], s[8:9], v5, s3, v[6:7]
	v_ashrrev_i32_e32 v5, 31, v4
	v_lshl_add_u64 v[4:5], v[6:7], 0, v[4:5]
	v_mad_u64_u32 v[12:13], s[8:9], v4, s13, v[8:9]
	s_mul_i32 s8, s14, 0x90
	s_barrier
	s_load_dwordx2 s[42:43], s[0:1], 0x8
	v_mov_b32_e32 v16, 0
	v_mov_b32_e32 v17, 0
	ds_write_b64 v16, v[16:17] offset:18112
	global_load_dwordx4 v[6:9], v[2:3], off
	v_mad_i32_i24 v13, v5, s13, v13
	v_ashrrev_i32_e32 v11, 31, v10
	v_lshl_add_u64 v[10:11], v[10:11], 4, v[12:13]
	global_load_dwordx4 v[10:13], v[10:11], off
	v_and_b32_e32 v1, 63, v0
	s_add_i32 s20, s8, s12
	s_lshl_b32 s20, s20, 10
	v_lshl_add_u32 v164, v1, 4, s20
	s_mul_i32 s9, s14, 0xbd
	s_add_i32 s21, s9, s18
	s_lshl_b32 s21, s21, 10
	v_lshl_add_u32 v165, v1, 4, s21
	s_add_u32 s22, s4, 0x1000
	s_addc_u32 s23, s5, 0
	s_add_u32 s24, s4, 0x2000
	s_addc_u32 s25, s5, 0
	s_mov_b32 s26, s6
	s_mov_b32 s27, s7
	s_add_u32 s28, s6, 0x1000
	s_addc_u32 s29, s7, 0
	s_add_u32 s30, s6, 0x2000
	s_addc_u32 s31, s7, 0
	s_add_u32 s32, s6, 0x3000
	s_addc_u32 s33, s7, 0
	s_add_u32 s34, s6, 0x4000
	s_addc_u32 s35, s7, 0
	s_add_u32 s36, s6, 0x5000
	s_addc_u32 s37, s7, 0
	v_bfe_u32 v166, v0, 4, 2
	v_and_b32_e32 v167, 15, v0
	v_lshlrev_b32_e32 v167, 3, v167
	s_mul_i32 s40, s15, 6
	s_mov_b32 s41, 0x7f000000
	global_load_dwordx4 v[112:115], v164, s[4:5]
	global_load_dwordx4 v[16:19], v165, s[26:27] nt
	global_load_dwordx4 v[20:23], v165, s[26:27] offset:1024 nt
	global_load_dwordx4 v[24:27], v165, s[26:27] offset:2048 nt
	global_load_dwordx4 v[28:31], v165, s[26:27] offset:3072 nt
	global_load_dwordx4 v[32:35], v165, s[28:29] nt
	global_load_dwordx4 v[36:39], v165, s[28:29] offset:1024 nt
	global_load_dwordx4 v[40:43], v165, s[28:29] offset:2048 nt
	global_load_dwordx4 v[44:47], v165, s[28:29] offset:3072 nt
	global_load_dwordx4 v[48:51], v165, s[30:31] nt
	global_load_dwordx4 v[52:55], v165, s[30:31] offset:1024 nt
	global_load_dwordx4 v[56:59], v165, s[30:31] offset:2048 nt
	global_load_dwordx4 v[60:63], v165, s[30:31] offset:3072 nt
	global_load_dwordx4 v[64:67], v165, s[32:33] nt
	global_load_dwordx4 v[68:71], v165, s[32:33] offset:1024 nt
	global_load_dwordx4 v[72:75], v165, s[32:33] offset:2048 nt
	global_load_dwordx4 v[76:79], v165, s[32:33] offset:3072 nt
	global_load_dwordx4 v[80:83], v165, s[34:35] nt
	global_load_dwordx4 v[84:87], v165, s[34:35] offset:1024 nt
	global_load_dwordx4 v[88:91], v165, s[34:35] offset:2048 nt
	global_load_dwordx4 v[92:95], v165, s[34:35] offset:3072 nt
	global_load_dwordx4 v[96:99], v165, s[36:37] nt
	global_load_dwordx4 v[100:103], v165, s[36:37] offset:1024 nt
	global_load_dwordx4 v[104:107], v165, s[36:37] offset:2048 nt
	global_load_dwordx4 v[108:111], v165, s[36:37] offset:3072 nt
	global_load_dwordx4 v[116:119], v164, s[4:5] offset:1024
	v_lshlrev_b32_e32 v14, 4, v0
	s_lshr_b32 s50, s15, 1
	s_and_b32 s51, s15, 1
	s_lshl_b32 s51, s51, 3
	s_mov_b32 s48, 0x1010101
	s_mov_b32 s49, 0x1010101
	s_movk_i32 s58, 0x900
	s_movk_i32 s59, 0xb40
	v_and_b32_e32 v168, 7, v0
	v_lshrrev_b32_e32 v177, 3, v1
	v_or_b32_e32 v177, s51, v177
	v_lshlrev_b32_e32 v169, 3, v177
	v_and_b32_e32 v179, 3, v0
	v_lshlrev_b32_e32 v179, 8, v179
	v_lshl_add_u32 v170, v177, 4, v179
	v_add_u32_e32 v170, s20, v170
	v_lshrrev_b32_e32 v179, 2, v168
	v_and_b32_e32 v180, 3, v0
	v_lshl_or_b32 v171, v179, 4, v180
	v_mul_u32_u24_e32 v179, 11, v168
	v_lshrrev_b32_e32 v179, 5, v179
	v_mul_u32_u24_e32 v180, 3, v179
	v_sub_u32_e32 v180, v168, v180
	v_mul_u32_u24_e32 v181, 0x90, v179
	v_add_u32_e32 v181, v181, v180
	v_mul_u32_u24_e32 v172, 0x240, v181
	v_mul_u32_u24_e32 v181, 0x48, v179
	v_add_u32_e32 v181, v181, v180
	v_mul_u32_u24_e32 v173, 0x120, v181
	v_mul_u32_u24_e32 v181, 0x24, v179
	v_add_u32_e32 v181, v181, v180
	v_mul_u32_u24_e32 v174, 0x90, v181
	v_mul_u32_u24_e32 v181, 9, v179
	v_add_u32_e32 v181, v181, v180
	v_mul_u32_u24_e32 v175, 0x240, v181
	v_add_u32_e32 v176, 8, v168
	s_waitcnt lgkmcnt(0)
	s_mul_i32 s60, s14, 0x3cc00
	s_add_u32 s42, s42, s60
	s_addc_u32 s43, s43, 0
	s_mul_i32 s60, s14, 0xf300
	s_add_u32 s44, s4, s60
	s_addc_u32 s45, s5, 0
	s_add_u32 s44, s44, 0x534000
	s_addc_u32 s45, s45, 0
	s_mul_i32 s60, s14, 0x3cc0
	s_add_u32 s46, s4, s60
	s_addc_u32 s47, s5, 0
	s_add_u32 s46, s46, 0x627000
	s_addc_u32 s47, s47, 0
	v_mov_b32_e32 v152, s42
	v_mov_b32_e32 v153, s43
	v_mov_b32_e32 v154, s44
	v_mov_b32_e32 v155, s45
	v_mov_b32_e32 v159, s46
	v_mov_b32_e32 v161, s47
	s_load_dwordx2 s[2:3], s[0:1], 0x18
	s_cmp_ge_u32 s15, 4
	s_cbranch_scc0 .Lprio_done
	s_setprio 1
.Lprio_done:
	s_waitcnt vmcnt(21)
	ds_write_b128 v14, v[6:9]
	ds_write_b128 v14, v[10:13] offset:8192
	v_mfma_f32_16x16x32_f16 v[120:123], v[16:19], v[112:115], 0
	v_mfma_f32_16x16x32_f16 v[124:127], v[20:23], v[112:115], 0
	v_mfma_f32_16x16x32_f16 v[128:131], v[24:27], v[112:115], 0
	v_mfma_f32_16x16x32_f16 v[132:135], v[28:31], v[112:115], 0
	s_waitcnt vmcnt(17)
	v_mfma_f32_16x16x32_f16 v[136:139], v[32:35], v[112:115], 0
	v_mfma_f32_16x16x32_f16 v[140:143], v[36:39], v[112:115], 0
	v_mfma_f32_16x16x32_f16 v[144:147], v[40:43], v[112:115], 0
	v_mfma_f32_16x16x32_f16 v[148:151], v[44:47], v[112:115], 0
	v_min3_i32 v160, v120, v121, s41
	v_min3_i32 v160, v122, v123, v160
	v_min3_i32 v160, v124, v125, v160
	v_min3_i32 v160, v126, v127, v160
	v_min3_i32 v160, v128, v129, v160
	v_min3_i32 v160, v130, v131, v160
	v_min3_i32 v160, v132, v133, v160
	v_min3_i32 v157, v134, v135, v160
	v_mov_b32_e32 v6, 0
	v_mov_b32_e32 v7, 0x900
	v_mov_b32_e32 v8, 0x240
	s_waitcnt vmcnt(13)
	v_mfma_f32_16x16x32_f16 v[120:123], v[48:51], v[112:115], 0
	v_mfma_f32_16x16x32_f16 v[124:127], v[52:55], v[112:115], 0
	v_mov_b32_e32 v158, 0
	v_mfma_f32_16x16x32_f16 v[128:131], v[56:59], v[112:115], 0
	v_mfma_f32_16x16x32_f16 v[132:135], v[60:63], v[112:115], 0
	v_min3_i32 v160, v136, v137, v157
	v_min3_i32 v160, v138, v139, v160
	v_min3_i32 v160, v140, v141, v160
	v_min3_i32 v160, v142, v143, v160
	v_min3_i32 v160, v144, v145, v160
	v_min3_i32 v160, v146, v147, v160
	v_min3_i32 v160, v148, v149, v160
	v_min3_i32 v156, v150, v151, v160
	v_cmp_ge_i32_e32 vcc, v156, v157
	s_waitcnt vmcnt(9)
	v_mfma_f32_16x16x32_f16 v[136:139], v[64:67], v[112:115], 0
	v_mfma_f32_16x16x32_f16 v[140:143], v[68:71], v[112:115], 0
	v_cndmask_b32_e32 v158, 1, v158, vcc
	v_mfma_f32_16x16x32_f16 v[144:147], v[72:75], v[112:115], 0
	v_mfma_f32_16x16x32_f16 v[148:151], v[76:79], v[112:115], 0
	v_min3_i32 v160, v120, v121, v156
	v_min3_i32 v160, v122, v123, v160
	v_min3_i32 v160, v124, v125, v160
	v_min3_i32 v160, v126, v127, v160
	v_min3_i32 v160, v128, v129, v160
	v_min3_i32 v160, v130, v131, v160
	v_min3_i32 v160, v132, v133, v160
	v_min3_i32 v157, v134, v135, v160
	v_cmp_ge_i32_e32 vcc, v157, v156
	s_waitcnt vmcnt(5)
	v_mfma_f32_16x16x32_f16 v[120:123], v[80:83], v[112:115], 0
	v_mfma_f32_16x16x32_f16 v[124:127], v[84:87], v[112:115], 0
	v_cndmask_b32_e32 v158, 2, v158, vcc
	v_mfma_f32_16x16x32_f16 v[128:131], v[88:91], v[112:115], 0
	v_mfma_f32_16x16x32_f16 v[132:135], v[92:95], v[112:115], 0
	v_min3_i32 v160, v136, v137, v157
	v_min3_i32 v160, v138, v139, v160
	v_min3_i32 v160, v140, v141, v160
	v_min3_i32 v160, v142, v143, v160
	v_min3_i32 v160, v144, v145, v160
	v_min3_i32 v160, v146, v147, v160
	v_min3_i32 v160, v148, v149, v160
	v_min3_i32 v156, v150, v151, v160
	v_cmp_ge_i32_e32 vcc, v156, v157
	s_waitcnt vmcnt(1)
	v_mfma_f32_16x16x32_f16 v[136:139], v[96:99], v[112:115], 0
	v_mfma_f32_16x16x32_f16 v[140:143], v[100:103], v[112:115], 0
	v_cndmask_b32_e32 v158, 3, v158, vcc
	v_mfma_f32_16x16x32_f16 v[144:147], v[104:107], v[112:115], 0
	v_mfma_f32_16x16x32_f16 v[148:151], v[108:111], v[112:115], 0
	v_min3_i32 v160, v120, v121, v156
	v_min3_i32 v160, v122, v123, v160
	v_min3_i32 v160, v124, v125, v160
	v_min3_i32 v160, v126, v127, v160
	v_min3_i32 v160, v128, v129, v160
	v_min3_i32 v160, v130, v131, v160
	v_min3_i32 v160, v132, v133, v160
	v_min3_i32 v157, v134, v135, v160
	v_cmp_ge_i32_e32 vcc, v157, v156
	s_waitcnt vmcnt(0)
	global_load_dwordx4 v[112:115], v164, s[4:5] offset:2048
	v_mfma_f32_16x16x32_f16 v[120:123], v[16:19], v[116:119], 0
	v_mfma_f32_16x16x32_f16 v[124:127], v[20:23], v[116:119], 0
	v_cndmask_b32_e32 v158, 4, v158, vcc
	v_mfma_f32_16x16x32_f16 v[128:131], v[24:27], v[116:119], 0
	v_mfma_f32_16x16x32_f16 v[132:135], v[28:31], v[116:119], 0
	v_min3_i32 v160, v136, v137, v157
	v_min3_i32 v160, v138, v139, v160
	v_min3_i32 v160, v140, v141, v160
	v_min3_i32 v160, v142, v143, v160
	v_min3_i32 v160, v144, v145, v160
	v_min3_i32 v160, v146, v147, v160
	v_min3_i32 v160, v148, v149, v160
	v_min3_i32 v156, v150, v151, v160
	v_cmp_ge_i32_e32 vcc, v156, v157
	v_mfma_f32_16x16x32_f16 v[136:139], v[32:35], v[116:119], 0
	v_mfma_f32_16x16x32_f16 v[140:143], v[36:39], v[116:119], 0
	v_cndmask_b32_e32 v158, 5, v158, vcc
	v_add_u32_e32 v162, s40, v158
	v_lshl_or_b32 v162, v162, 2, v166
	v_mov_b32_e32 v163, v156
	ds_min_u64 v167, v[162:163] offset:16384
	v_mfma_f32_16x16x32_f16 v[144:147], v[40:43], v[116:119], 0
	v_mfma_f32_16x16x32_f16 v[148:151], v[44:47], v[116:119], 0
	v_min3_i32 v160, v120, v121, s41
	v_min3_i32 v160, v122, v123, v160
	v_min3_i32 v160, v124, v125, v160
	v_min3_i32 v160, v126, v127, v160
	v_min3_i32 v160, v128, v129, v160
	v_min3_i32 v160, v130, v131, v160
	v_min3_i32 v160, v132, v133, v160
	v_min3_i32 v157, v134, v135, v160
	v_mfma_f32_16x16x32_f16 v[120:123], v[48:51], v[116:119], 0
	v_mfma_f32_16x16x32_f16 v[124:127], v[52:55], v[116:119], 0
	v_mov_b32_e32 v158, 0
	v_mfma_f32_16x16x32_f16 v[128:131], v[56:59], v[116:119], 0
	v_mfma_f32_16x16x32_f16 v[132:135], v[60:63], v[116:119], 0
	v_min3_i32 v160, v136, v137, v157
	v_min3_i32 v160, v138, v139, v160
	v_min3_i32 v160, v140, v141, v160
	v_min3_i32 v160, v142, v143, v160
	v_min3_i32 v160, v144, v145, v160
	v_min3_i32 v160, v146, v147, v160
	v_min3_i32 v160, v148, v149, v160
	v_min3_i32 v156, v150, v151, v160
	v_cmp_ge_i32_e32 vcc, v156, v157
	v_mfma_f32_16x16x32_f16 v[136:139], v[64:67], v[116:119], 0
	v_mfma_f32_16x16x32_f16 v[140:143], v[68:71], v[116:119], 0
	v_cndmask_b32_e32 v158, 1, v158, vcc
	v_mfma_f32_16x16x32_f16 v[144:147], v[72:75], v[116:119], 0
	v_mfma_f32_16x16x32_f16 v[148:151], v[76:79], v[116:119], 0
	v_min3_i32 v160, v120, v121, v156
	v_min3_i32 v160, v122, v123, v160
	v_min3_i32 v160, v124, v125, v160
	v_min3_i32 v160, v126, v127, v160
	v_min3_i32 v160, v128, v129, v160
	v_min3_i32 v160, v130, v131, v160
	v_min3_i32 v160, v132, v133, v160
	v_min3_i32 v157, v134, v135, v160
	v_cmp_ge_i32_e32 vcc, v157, v156
	v_mfma_f32_16x16x32_f16 v[120:123], v[80:83], v[116:119], 0
	v_mfma_f32_16x16x32_f16 v[124:127], v[84:87], v[116:119], 0
	v_cndmask_b32_e32 v158, 2, v158, vcc
	v_mfma_f32_16x16x32_f16 v[128:131], v[88:91], v[116:119], 0
	v_mfma_f32_16x16x32_f16 v[132:135], v[92:95], v[116:119], 0
	v_min3_i32 v160, v136, v137, v157
	v_min3_i32 v160, v138, v139, v160
	v_min3_i32 v160, v140, v141, v160
	v_min3_i32 v160, v142, v143, v160
	v_min3_i32 v160, v144, v145, v160
	v_min3_i32 v160, v146, v147, v160
	v_min3_i32 v160, v148, v149, v160
	v_min3_i32 v156, v150, v151, v160
	v_cmp_ge_i32_e32 vcc, v156, v157
	v_mfma_f32_16x16x32_f16 v[136:139], v[96:99], v[116:119], 0
	v_mfma_f32_16x16x32_f16 v[140:143], v[100:103], v[116:119], 0
	v_cndmask_b32_e32 v158, 3, v158, vcc
	v_mfma_f32_16x16x32_f16 v[144:147], v[104:107], v[116:119], 0
	v_mfma_f32_16x16x32_f16 v[148:151], v[108:111], v[116:119], 0
	v_min3_i32 v160, v120, v121, v156
	v_min3_i32 v160, v122, v123, v160
	v_min3_i32 v160, v124, v125, v160
	v_min3_i32 v160, v126, v127, v160
	v_min3_i32 v160, v128, v129, v160
	v_min3_i32 v160, v130, v131, v160
	v_min3_i32 v160, v132, v133, v160
	v_min3_i32 v157, v134, v135, v160
	v_cmp_ge_i32_e32 vcc, v157, v156
	s_waitcnt vmcnt(0)
	global_load_dwordx4 v[116:119], v164, s[4:5] offset:3072
	v_mfma_f32_16x16x32_f16 v[120:123], v[16:19], v[112:115], 0
	v_mfma_f32_16x16x32_f16 v[124:127], v[20:23], v[112:115], 0
	v_cndmask_b32_e32 v158, 4, v158, vcc
	v_mfma_f32_16x16x32_f16 v[128:131], v[24:27], v[112:115], 0
	v_mfma_f32_16x16x32_f16 v[132:135], v[28:31], v[112:115], 0
	v_min3_i32 v160, v136, v137, v157
	v_min3_i32 v160, v138, v139, v160
	v_min3_i32 v160, v140, v141, v160
	v_min3_i32 v160, v142, v143, v160
	v_min3_i32 v160, v144, v145, v160
	v_min3_i32 v160, v146, v147, v160
	v_min3_i32 v160, v148, v149, v160
	v_min3_i32 v156, v150, v151, v160
	v_cmp_ge_i32_e32 vcc, v156, v157
	v_mfma_f32_16x16x32_f16 v[136:139], v[32:35], v[112:115], 0
	v_mfma_f32_16x16x32_f16 v[140:143], v[36:39], v[112:115], 0
	v_cndmask_b32_e32 v158, 5, v158, vcc
	v_add_u32_e32 v162, s40, v158
	v_lshl_or_b32 v162, v162, 2, v166
	v_mov_b32_e32 v163, v156
	ds_min_u64 v167, v[162:163] offset:16512
	v_mfma_f32_16x16x32_f16 v[144:147], v[40:43], v[112:115], 0
	v_mfma_f32_16x16x32_f16 v[148:151], v[44:47], v[112:115], 0
	v_min3_i32 v160, v120, v121, s41
	v_min3_i32 v160, v122, v123, v160
	v_min3_i32 v160, v124, v125, v160
	v_min3_i32 v160, v126, v127, v160
	v_min3_i32 v160, v128, v129, v160
	v_min3_i32 v160, v130, v131, v160
	v_min3_i32 v160, v132, v133, v160
	v_min3_i32 v157, v134, v135, v160
	v_mfma_f32_16x16x32_f16 v[120:123], v[48:51], v[112:115], 0
	v_mfma_f32_16x16x32_f16 v[124:127], v[52:55], v[112:115], 0
	v_mov_b32_e32 v158, 0
	v_mfma_f32_16x16x32_f16 v[128:131], v[56:59], v[112:115], 0
	v_mfma_f32_16x16x32_f16 v[132:135], v[60:63], v[112:115], 0
	v_min3_i32 v160, v136, v137, v157
	v_min3_i32 v160, v138, v139, v160
	v_min3_i32 v160, v140, v141, v160
	v_min3_i32 v160, v142, v143, v160
	v_min3_i32 v160, v144, v145, v160
	v_min3_i32 v160, v146, v147, v160
	v_min3_i32 v160, v148, v149, v160
	v_min3_i32 v156, v150, v151, v160
	v_cmp_ge_i32_e32 vcc, v156, v157
	v_mfma_f32_16x16x32_f16 v[136:139], v[64:67], v[112:115], 0
	v_mfma_f32_16x16x32_f16 v[140:143], v[68:71], v[112:115], 0
	v_cndmask_b32_e32 v158, 1, v158, vcc
	v_mfma_f32_16x16x32_f16 v[144:147], v[72:75], v[112:115], 0
	v_mfma_f32_16x16x32_f16 v[148:151], v[76:79], v[112:115], 0
	v_min3_i32 v160, v120, v121, v156
	v_min3_i32 v160, v122, v123, v160
	v_min3_i32 v160, v124, v125, v160
	v_min3_i32 v160, v126, v127, v160
	v_min3_i32 v160, v128, v129, v160
	v_min3_i32 v160, v130, v131, v160
	v_min3_i32 v160, v132, v133, v160
	v_min3_i32 v157, v134, v135, v160
	v_cmp_ge_i32_e32 vcc, v157, v156
	v_mfma_f32_16x16x32_f16 v[120:123], v[80:83], v[112:115], 0
	v_mfma_f32_16x16x32_f16 v[124:127], v[84:87], v[112:115], 0
	v_cndmask_b32_e32 v158, 2, v158, vcc
	v_mfma_f32_16x16x32_f16 v[128:131], v[88:91], v[112:115], 0
	v_mfma_f32_16x16x32_f16 v[132:135], v[92:95], v[112:115], 0
	v_min3_i32 v160, v136, v137, v157
	v_min3_i32 v160, v138, v139, v160
	v_min3_i32 v160, v140, v141, v160
	v_min3_i32 v160, v142, v143, v160
	v_min3_i32 v160, v144, v145, v160
	v_min3_i32 v160, v146, v147, v160
	v_min3_i32 v160, v148, v149, v160
	v_min3_i32 v156, v150, v151, v160
	v_cmp_ge_i32_e32 vcc, v156, v157
	v_mfma_f32_16x16x32_f16 v[136:139], v[96:99], v[112:115], 0
	v_mfma_f32_16x16x32_f16 v[140:143], v[100:103], v[112:115], 0
	v_cndmask_b32_e32 v158, 3, v158, vcc
	v_mfma_f32_16x16x32_f16 v[144:147], v[104:107], v[112:115], 0
	v_mfma_f32_16x16x32_f16 v[148:151], v[108:111], v[112:115], 0
	v_min3_i32 v160, v120, v121, v156
	v_min3_i32 v160, v122, v123, v160
	v_min3_i32 v160, v124, v125, v160
	v_min3_i32 v160, v126, v127, v160
	v_min3_i32 v160, v128, v129, v160
	v_min3_i32 v160, v130, v131, v160
	v_min3_i32 v160, v132, v133, v160
	v_min3_i32 v157, v134, v135, v160
	v_cmp_ge_i32_e32 vcc, v157, v156
	s_waitcnt vmcnt(0)
	global_load_dwordx4 v[112:115], v164, s[22:23]
	v_mfma_f32_16x16x32_f16 v[120:123], v[16:19], v[116:119], 0
	v_mfma_f32_16x16x32_f16 v[124:127], v[20:23], v[116:119], 0
	v_cndmask_b32_e32 v158, 4, v158, vcc
	v_mfma_f32_16x16x32_f16 v[128:131], v[24:27], v[116:119], 0
	v_mfma_f32_16x16x32_f16 v[132:135], v[28:31], v[116:119], 0
	v_min3_i32 v160, v136, v137, v157
	v_min3_i32 v160, v138, v139, v160
	v_min3_i32 v160, v140, v141, v160
	v_min3_i32 v160, v142, v143, v160
	v_min3_i32 v160, v144, v145, v160
	v_min3_i32 v160, v146, v147, v160
	v_min3_i32 v160, v148, v149, v160
	v_min3_i32 v156, v150, v151, v160
	v_cmp_ge_i32_e32 vcc, v156, v157
	v_mfma_f32_16x16x32_f16 v[136:139], v[32:35], v[116:119], 0
	v_mfma_f32_16x16x32_f16 v[140:143], v[36:39], v[116:119], 0
	v_cndmask_b32_e32 v158, 5, v158, vcc
	v_add_u32_e32 v162, s40, v158
	v_lshl_or_b32 v162, v162, 2, v166
	v_mov_b32_e32 v163, v156
	ds_min_u64 v167, v[162:163] offset:16640
	v_mfma_f32_16x16x32_f16 v[144:147], v[40:43], v[116:119], 0
	v_mfma_f32_16x16x32_f16 v[148:151], v[44:47], v[116:119], 0
	v_min3_i32 v160, v120, v121, s41
	v_min3_i32 v160, v122, v123, v160
	v_min3_i32 v160, v124, v125, v160
	v_min3_i32 v160, v126, v127, v160
	v_min3_i32 v160, v128, v129, v160
	v_min3_i32 v160, v130, v131, v160
	v_min3_i32 v160, v132, v133, v160
	v_min3_i32 v157, v134, v135, v160
	v_mfma_f32_16x16x32_f16 v[120:123], v[48:51], v[116:119], 0
	v_mfma_f32_16x16x32_f16 v[124:127], v[52:55], v[116:119], 0
	v_mov_b32_e32 v158, 0
	v_mfma_f32_16x16x32_f16 v[128:131], v[56:59], v[116:119], 0
	v_mfma_f32_16x16x32_f16 v[132:135], v[60:63], v[116:119], 0
	v_min3_i32 v160, v136, v137, v157
	v_min3_i32 v160, v138, v139, v160
	v_min3_i32 v160, v140, v141, v160
	v_min3_i32 v160, v142, v143, v160
	v_min3_i32 v160, v144, v145, v160
	v_min3_i32 v160, v146, v147, v160
	v_min3_i32 v160, v148, v149, v160
	v_min3_i32 v156, v150, v151, v160
	v_cmp_ge_i32_e32 vcc, v156, v157
	v_mfma_f32_16x16x32_f16 v[136:139], v[64:67], v[116:119], 0
	v_mfma_f32_16x16x32_f16 v[140:143], v[68:71], v[116:119], 0
	v_cndmask_b32_e32 v158, 1, v158, vcc
	v_mfma_f32_16x16x32_f16 v[144:147], v[72:75], v[116:119], 0
	v_mfma_f32_16x16x32_f16 v[148:151], v[76:79], v[116:119], 0
	v_min3_i32 v160, v120, v121, v156
	v_min3_i32 v160, v122, v123, v160
	v_min3_i32 v160, v124, v125, v160
	v_min3_i32 v160, v126, v127, v160
	v_min3_i32 v160, v128, v129, v160
	v_min3_i32 v160, v130, v131, v160
	v_min3_i32 v160, v132, v133, v160
	v_min3_i32 v157, v134, v135, v160
	v_cmp_ge_i32_e32 vcc, v157, v156
	v_mfma_f32_16x16x32_f16 v[120:123], v[80:83], v[116:119], 0
	v_mfma_f32_16x16x32_f16 v[124:127], v[84:87], v[116:119], 0
	v_cndmask_b32_e32 v158, 2, v158, vcc
	v_mfma_f32_16x16x32_f16 v[128:131], v[88:91], v[116:119], 0
	v_mfma_f32_16x16x32_f16 v[132:135], v[92:95], v[116:119], 0
	v_min3_i32 v160, v136, v137, v157
	v_min3_i32 v160, v138, v139, v160
	v_min3_i32 v160, v140, v141, v160
	v_min3_i32 v160, v142, v143, v160
	v_min3_i32 v160, v144, v145, v160
	v_min3_i32 v160, v146, v147, v160
	v_min3_i32 v160, v148, v149, v160
	v_min3_i32 v156, v150, v151, v160
	v_cmp_ge_i32_e32 vcc, v156, v157
	v_mfma_f32_16x16x32_f16 v[136:139], v[96:99], v[116:119], 0
	v_mfma_f32_16x16x32_f16 v[140:143], v[100:103], v[116:119], 0
	v_cndmask_b32_e32 v158, 3, v158, vcc
	v_mfma_f32_16x16x32_f16 v[144:147], v[104:107], v[116:119], 0
	v_mfma_f32_16x16x32_f16 v[148:151], v[108:111], v[116:119], 0
	v_min3_i32 v160, v120, v121, v156
	v_min3_i32 v160, v122, v123, v160
	v_min3_i32 v160, v124, v125, v160
	v_min3_i32 v160, v126, v127, v160
	v_min3_i32 v160, v128, v129, v160
	v_min3_i32 v160, v130, v131, v160
	v_min3_i32 v160, v132, v133, v160
	v_min3_i32 v157, v134, v135, v160
	v_cmp_ge_i32_e32 vcc, v157, v156
	s_waitcnt vmcnt(0)
	global_load_dwordx4 v[116:119], v164, s[22:23] offset:1024
	v_mfma_f32_16x16x32_f16 v[120:123], v[16:19], v[112:115], 0
	v_mfma_f32_16x16x32_f16 v[124:127], v[20:23], v[112:115], 0
	v_cndmask_b32_e32 v158, 4, v158, vcc
	v_mfma_f32_16x16x32_f16 v[128:131], v[24:27], v[112:115], 0
	v_mfma_f32_16x16x32_f16 v[132:135], v[28:31], v[112:115], 0
	v_min3_i32 v160, v136, v137, v157
	v_min3_i32 v160, v138, v139, v160
	v_min3_i32 v160, v140, v141, v160
	v_min3_i32 v160, v142, v143, v160
	v_min3_i32 v160, v144, v145, v160
	v_min3_i32 v160, v146, v147, v160
	v_min3_i32 v160, v148, v149, v160
	v_min3_i32 v156, v150, v151, v160
	v_cmp_ge_i32_e32 vcc, v156, v157
	v_mfma_f32_16x16x32_f16 v[136:139], v[32:35], v[112:115], 0
	v_mfma_f32_16x16x32_f16 v[140:143], v[36:39], v[112:115], 0
	v_cndmask_b32_e32 v158, 5, v158, vcc
	v_add_u32_e32 v162, s40, v158
	v_lshl_or_b32 v162, v162, 2, v166
	v_mov_b32_e32 v163, v156
	ds_min_u64 v167, v[162:163] offset:16768
	v_mfma_f32_16x16x32_f16 v[144:147], v[40:43], v[112:115], 0
	v_mfma_f32_16x16x32_f16 v[148:151], v[44:47], v[112:115], 0
	v_min3_i32 v160, v120, v121, s41
	v_min3_i32 v160, v122, v123, v160
	v_min3_i32 v160, v124, v125, v160
	v_min3_i32 v160, v126, v127, v160
	v_min3_i32 v160, v128, v129, v160
	v_min3_i32 v160, v130, v131, v160
	v_min3_i32 v160, v132, v133, v160
	v_min3_i32 v157, v134, v135, v160
	v_mfma_f32_16x16x32_f16 v[120:123], v[48:51], v[112:115], 0
	v_mfma_f32_16x16x32_f16 v[124:127], v[52:55], v[112:115], 0
	v_mov_b32_e32 v158, 0
	v_mfma_f32_16x16x32_f16 v[128:131], v[56:59], v[112:115], 0
	v_mfma_f32_16x16x32_f16 v[132:135], v[60:63], v[112:115], 0
	v_min3_i32 v160, v136, v137, v157
	v_min3_i32 v160, v138, v139, v160
	v_min3_i32 v160, v140, v141, v160
	v_min3_i32 v160, v142, v143, v160
	v_min3_i32 v160, v144, v145, v160
	v_min3_i32 v160, v146, v147, v160
	v_min3_i32 v160, v148, v149, v160
	v_min3_i32 v156, v150, v151, v160
	v_cmp_ge_i32_e32 vcc, v156, v157
	v_mfma_f32_16x16x32_f16 v[136:139], v[64:67], v[112:115], 0
	v_mfma_f32_16x16x32_f16 v[140:143], v[68:71], v[112:115], 0
	v_cndmask_b32_e32 v158, 1, v158, vcc
	v_mfma_f32_16x16x32_f16 v[144:147], v[72:75], v[112:115], 0
	v_mfma_f32_16x16x32_f16 v[148:151], v[76:79], v[112:115], 0
	v_min3_i32 v160, v120, v121, v156
	v_min3_i32 v160, v122, v123, v160
	v_min3_i32 v160, v124, v125, v160
	v_min3_i32 v160, v126, v127, v160
	v_min3_i32 v160, v128, v129, v160
	v_min3_i32 v160, v130, v131, v160
	v_min3_i32 v160, v132, v133, v160
	v_min3_i32 v157, v134, v135, v160
	v_cmp_ge_i32_e32 vcc, v157, v156
	v_mfma_f32_16x16x32_f16 v[120:123], v[80:83], v[112:115], 0
	v_mfma_f32_16x16x32_f16 v[124:127], v[84:87], v[112:115], 0
	v_cndmask_b32_e32 v158, 2, v158, vcc
	v_mfma_f32_16x16x32_f16 v[128:131], v[88:91], v[112:115], 0
	v_mfma_f32_16x16x32_f16 v[132:135], v[92:95], v[112:115], 0
	v_min3_i32 v160, v136, v137, v157
	v_min3_i32 v160, v138, v139, v160
	v_min3_i32 v160, v140, v141, v160
	v_min3_i32 v160, v142, v143, v160
	v_min3_i32 v160, v144, v145, v160
	v_min3_i32 v160, v146, v147, v160
	v_min3_i32 v160, v148, v149, v160
	v_min3_i32 v156, v150, v151, v160
	v_cmp_ge_i32_e32 vcc, v156, v157
	v_mfma_f32_16x16x32_f16 v[136:139], v[96:99], v[112:115], 0
	v_mfma_f32_16x16x32_f16 v[140:143], v[100:103], v[112:115], 0
	v_cndmask_b32_e32 v158, 3, v158, vcc
	v_mfma_f32_16x16x32_f16 v[144:147], v[104:107], v[112:115], 0
	v_mfma_f32_16x16x32_f16 v[148:151], v[108:111], v[112:115], 0
	v_min3_i32 v160, v120, v121, v156
	v_min3_i32 v160, v122, v123, v160
	v_min3_i32 v160, v124, v125, v160
	v_min3_i32 v160, v126, v127, v160
	v_min3_i32 v160, v128, v129, v160
	v_min3_i32 v160, v130, v131, v160
	v_min3_i32 v160, v132, v133, v160
	v_min3_i32 v157, v134, v135, v160
	v_cmp_ge_i32_e32 vcc, v157, v156
	s_waitcnt vmcnt(0)
	global_load_dwordx4 v[112:115], v164, s[22:23] offset:2048
	v_mfma_f32_16x16x32_f16 v[120:123], v[16:19], v[116:119], 0
	v_mfma_f32_16x16x32_f16 v[124:127], v[20:23], v[116:119], 0
	v_cndmask_b32_e32 v158, 4, v158, vcc
	v_mfma_f32_16x16x32_f16 v[128:131], v[24:27], v[116:119], 0
	v_mfma_f32_16x16x32_f16 v[132:135], v[28:31], v[116:119], 0
	v_min3_i32 v160, v136, v137, v157
	v_min3_i32 v160, v138, v139, v160
	v_min3_i32 v160, v140, v141, v160
	v_min3_i32 v160, v142, v143, v160
	v_min3_i32 v160, v144, v145, v160
	v_min3_i32 v160, v146, v147, v160
	v_min3_i32 v160, v148, v149, v160
	v_min3_i32 v156, v150, v151, v160
	v_cmp_ge_i32_e32 vcc, v156, v157
	v_mfma_f32_16x16x32_f16 v[136:139], v[32:35], v[116:119], 0
	v_mfma_f32_16x16x32_f16 v[140:143], v[36:39], v[116:119], 0
	v_cndmask_b32_e32 v158, 5, v158, vcc
	v_add_u32_e32 v162, s40, v158
	v_lshl_or_b32 v162, v162, 2, v166
	v_mov_b32_e32 v163, v156
	ds_min_u64 v167, v[162:163] offset:16896
	v_mfma_f32_16x16x32_f16 v[144:147], v[40:43], v[116:119], 0
	v_mfma_f32_16x16x32_f16 v[148:151], v[44:47], v[116:119], 0
	v_min3_i32 v160, v120, v121, s41
	v_min3_i32 v160, v122, v123, v160
	v_min3_i32 v160, v124, v125, v160
	v_min3_i32 v160, v126, v127, v160
	v_min3_i32 v160, v128, v129, v160
	v_min3_i32 v160, v130, v131, v160
	v_min3_i32 v160, v132, v133, v160
	v_min3_i32 v157, v134, v135, v160
	v_mfma_f32_16x16x32_f16 v[120:123], v[48:51], v[116:119], 0
	v_mfma_f32_16x16x32_f16 v[124:127], v[52:55], v[116:119], 0
	v_mov_b32_e32 v158, 0
	v_mfma_f32_16x16x32_f16 v[128:131], v[56:59], v[116:119], 0
	v_mfma_f32_16x16x32_f16 v[132:135], v[60:63], v[116:119], 0
	v_min3_i32 v160, v136, v137, v157
	v_min3_i32 v160, v138, v139, v160
	v_min3_i32 v160, v140, v141, v160
	v_min3_i32 v160, v142, v143, v160
	v_min3_i32 v160, v144, v145, v160
	v_min3_i32 v160, v146, v147, v160
	v_min3_i32 v160, v148, v149, v160
	v_min3_i32 v156, v150, v151, v160
	v_cmp_ge_i32_e32 vcc, v156, v157
	v_mfma_f32_16x16x32_f16 v[136:139], v[64:67], v[116:119], 0
	v_mfma_f32_16x16x32_f16 v[140:143], v[68:71], v[116:119], 0
	v_cndmask_b32_e32 v158, 1, v158, vcc
	v_mfma_f32_16x16x32_f16 v[144:147], v[72:75], v[116:119], 0
	v_mfma_f32_16x16x32_f16 v[148:151], v[76:79], v[116:119], 0
	v_min3_i32 v160, v120, v121, v156
	v_min3_i32 v160, v122, v123, v160
	v_min3_i32 v160, v124, v125, v160
	v_min3_i32 v160, v126, v127, v160
	v_min3_i32 v160, v128, v129, v160
	v_min3_i32 v160, v130, v131, v160
	v_min3_i32 v160, v132, v133, v160
	v_min3_i32 v157, v134, v135, v160
	v_cmp_ge_i32_e32 vcc, v157, v156
	v_mfma_f32_16x16x32_f16 v[120:123], v[80:83], v[116:119], 0
	v_mfma_f32_16x16x32_f16 v[124:127], v[84:87], v[116:119], 0
	v_cndmask_b32_e32 v158, 2, v158, vcc
	v_mfma_f32_16x16x32_f16 v[128:131], v[88:91], v[116:119], 0
	v_mfma_f32_16x16x32_f16 v[132:135], v[92:95], v[116:119], 0
	v_min3_i32 v160, v136, v137, v157
	v_min3_i32 v160, v138, v139, v160
	v_min3_i32 v160, v140, v141, v160
	v_min3_i32 v160, v142, v143, v160
	v_min3_i32 v160, v144, v145, v160
	v_min3_i32 v160, v146, v147, v160
	v_min3_i32 v160, v148, v149, v160
	v_min3_i32 v156, v150, v151, v160
	v_cmp_ge_i32_e32 vcc, v156, v157
	v_mfma_f32_16x16x32_f16 v[136:139], v[96:99], v[116:119], 0
	v_mfma_f32_16x16x32_f16 v[140:143], v[100:103], v[116:119], 0
	v_cndmask_b32_e32 v158, 3, v158, vcc
	v_mfma_f32_16x16x32_f16 v[144:147], v[104:107], v[116:119], 0
	v_mfma_f32_16x16x32_f16 v[148:151], v[108:111], v[116:119], 0
	v_min3_i32 v160, v120, v121, v156
	v_min3_i32 v160, v122, v123, v160
	v_min3_i32 v160, v124, v125, v160
	v_min3_i32 v160, v126, v127, v160
	v_min3_i32 v160, v128, v129, v160
	v_min3_i32 v160, v130, v131, v160
	v_min3_i32 v160, v132, v133, v160
	v_min3_i32 v157, v134, v135, v160
	v_cmp_ge_i32_e32 vcc, v157, v156
	s_waitcnt vmcnt(0)
	global_load_dwordx4 v[116:119], v164, s[22:23] offset:3072
	v_mfma_f32_16x16x32_f16 v[120:123], v[16:19], v[112:115], 0
	v_mfma_f32_16x16x32_f16 v[124:127], v[20:23], v[112:115], 0
	v_cndmask_b32_e32 v158, 4, v158, vcc
	v_mfma_f32_16x16x32_f16 v[128:131], v[24:27], v[112:115], 0
	v_mfma_f32_16x16x32_f16 v[132:135], v[28:31], v[112:115], 0
	v_min3_i32 v160, v136, v137, v157
	v_min3_i32 v160, v138, v139, v160
	v_min3_i32 v160, v140, v141, v160
	v_min3_i32 v160, v142, v143, v160
	v_min3_i32 v160, v144, v145, v160
	v_min3_i32 v160, v146, v147, v160
	v_min3_i32 v160, v148, v149, v160
	v_min3_i32 v156, v150, v151, v160
	v_cmp_ge_i32_e32 vcc, v156, v157
	v_mfma_f32_16x16x32_f16 v[136:139], v[32:35], v[112:115], 0
	v_mfma_f32_16x16x32_f16 v[140:143], v[36:39], v[112:115], 0
	v_cndmask_b32_e32 v158, 5, v158, vcc
	v_add_u32_e32 v162, s40, v158
	v_lshl_or_b32 v162, v162, 2, v166
	v_mov_b32_e32 v163, v156
	ds_min_u64 v167, v[162:163] offset:17024
	v_mfma_f32_16x16x32_f16 v[144:147], v[40:43], v[112:115], 0
	v_mfma_f32_16x16x32_f16 v[148:151], v[44:47], v[112:115], 0
	v_min3_i32 v160, v120, v121, s41
	v_min3_i32 v160, v122, v123, v160
	v_min3_i32 v160, v124, v125, v160
	v_min3_i32 v160, v126, v127, v160
	v_min3_i32 v160, v128, v129, v160
	v_min3_i32 v160, v130, v131, v160
	v_min3_i32 v160, v132, v133, v160
	v_min3_i32 v157, v134, v135, v160
	s_waitcnt lgkmcnt(0)
	s_barrier
	s_lshl_b32 s60, s50, 7
	v_add_u32_e32 v2, s60, v169
	ds_read_b32 v178, v2 offset:16384
	s_lshl_b32 s60, s50, 10
	v_add_u32_e32 v210, s60, v170
	s_cmp_lt_u32 s50, 2
	s_cbranch_scc0 .Lp1a_y
	s_add_i32 s65, s50, 4
	s_lshl_b32 s60, s65, 7
	v_add_u32_e32 v2, s60, v169
	ds_read_b32 v216, v2 offset:16384
	s_lshl_b32 s60, s65, 10
	v_add_u32_e32 v248, s60, v170
